# norm2 row pass: next trip's 12 loads prefetched into a second register set at the start of each trip
# baseline (speedup 1.0000x reference)
; template <class Tp> __device__ __forceinline__ Tp* wsp(const Frame& F, size_t off) { return (Tp*)(F.ws + off); }
; __device__ __forceinline__ void phase_norm2(Frame& F, int l, float ysc) {
;     bf16_t* HB = wsp<bf16_t>(F, WS_HB); float* RS = wsp<float>(F, WS_RS); const bf16_t* Y = wsp<bf16_t>(F, WS_Y);
;     for (int row0 = 2 * F.gw(); row0 < T; row0 += 2 * F.ngw()) {
;         u32x4 hw[2][2], ya[2][2], yb[2][2];
; #pragma unroll
;         for (int q = 0; q < 2; ++q) { const u32x4* xr = (const u32x4*)(HB + (size_t)(row0 + q) * DM) + F.lane; const u32x4* y0 = (const u32x4*)(Y + (size_t)(row0 + q) * 2 * DM) + F.lane; const u32x4* y1 = y0 + DM / 8;
; #pragma unroll
;             for (int j = 0; j < 2; ++j) { hw[q][j] = xr[64 * j]; ya[q][j] = y0[64 * j]; yb[q][j] = y1[64 * j]; } }
.LBB0_1418:
	s_or_b64 exec, exec, s[44:45]
	v_readlane_b32 s2, v253, 4
	v_readlane_b32 s3, v253, 5
	s_andn2_b64 vcc, exec, s[2:3]
	s_waitcnt lgkmcnt(0)
	s_barrier
	s_cbranch_vccnz .LBB0_1425
	v_and_b32_e32 v0, 63, v188
	v_readlane_b32 s2, v254, 39
	v_cmp_eq_u32_e64 s[10:11], 0, v0
	v_lshlrev_b32_e32 v0, 4, v0
	v_readlane_b32 s3, v254, 40
	v_readlane_b32 s14, v254, 35
	v_readlane_b32 s15, v254, 36
	v_lshl_add_u64 v[38:39], s[2:3], 0, v[0:1]
	v_readlane_b32 s2, v254, 45
	v_readlane_b32 s3, v254, 46
	s_nop 1
	v_lshl_add_u64 v[40:41], s[2:3], 0, v[0:1]
	v_readlane_b32 s2, v254, 43
	v_readlane_b32 s3, v254, 44
	v_lshl_add_u64 v[116:117], s[74:75], 0, v[40:41]
	v_add_co_u32_e32 v116, vcc, 0xee00000, v116
	s_nop 1
	v_addc_co_u32_e32 v117, vcc, 0, v117, vcc
	v_lshl_add_u64 v[122:123], s[74:75], 0, v[38:39]
	v_add_co_u32_e32 v124, vcc, 0x15200000, v122
	s_nop 1
	v_addc_co_u32_e32 v125, vcc, 0, v123, vcc
	s_mov_b32 s3, 0x15201000
	v_add_co_u32_e32 v126, vcc, s3, v122
	s_nop 1
	v_addc_co_u32_e32 v127, vcc, 0, v123, vcc
	global_load_dwordx4 v[64:67], v[116:117], off
	global_load_dwordx4 v[68:71], v[124:125], off
	global_load_dwordx4 v[72:75], v[124:125], off offset:2048
	global_load_dwordx4 v[76:79], v[116:117], off offset:1024
	global_load_dwordx4 v[80:83], v[124:125], off offset:1024
	global_load_dwordx4 v[84:87], v[124:125], off offset:3072
	global_load_dwordx4 v[88:91], v[116:117], off offset:2048
	global_load_dwordx4 v[92:95], v[126:127], off
	global_load_dwordx4 v[98:101], v[126:127], off offset:2048
	global_load_dwordx4 v[102:105], v[116:117], off offset:3072
	global_load_dwordx4 v[106:109], v[126:127], off offset:1024
	global_load_dwordx4 v[110:113], v[126:127], off offset:3072
	s_waitcnt vmcnt(0)
	s_branch .Ln2_enter

; __device__ __forceinline__ unsigned pk2(float lo, float hi) { f32x2_cv_ v = {lo, hi}; return __builtin_bit_cast(unsigned, __builtin_convertvector(v, bf16x2_cv_)); }
; __device__ __forceinline__ void phase_norm2(Frame& F, int l, float ysc) {
;     ...
;     for (int row0 = 2 * F.gw(); row0 < T; row0 += 2 * F.ngw()) {
;         u32x4 hw[2][2], ya[2][2], yb[2][2];
; #pragma unroll
;         for (int q = 0; q < 2; ++q) { const u32x4* xr = (const u32x4*)(HB + (size_t)(row0 + q) * DM) + F.lane; const u32x4* y0 = (const u32x4*)(Y + (size_t)(row0 + q) * 2 * DM) + F.lane; const u32x4* y1 = y0 + DM / 8;
; #pragma unroll
;             for (int j = 0; j < 2; ++j) { hw[q][j] = xr[64 * j]; ya[q][j] = y0[64 * j]; yb[q][j] = y1[64 * j]; } }
; #pragma unroll
;         for (int q = 0; q < 2; ++q) { float s = 0.f; u32x4* xr = (u32x4*)(HB + (size_t)(row0 + q) * DM) + F.lane;
; #pragma unroll
;             for (int j = 0; j < 2; ++j) { float h[8], a[8], b[8]; unpack8(hw[q][j], h); unpack8(ya[q][j], a); unpack8(yb[q][j], b);
; #pragma unroll
;                 for (int i = 0; i < 8; ++i) h[i] += ysc * (a[i] + b[i]);
;                 const u32x4 o = (u32x4){pk2(h[0], h[1]), pk2(h[2], h[3]), pk2(h[4], h[5]), pk2(h[6], h[7])}; xr[64 * j] = o;
;                 unpack8(o, h);
; #pragma unroll
;                 for (int i = 0; i < 8; i += 4) s += (h[i] * h[i] + h[i + 1] * h[i + 1]) + (h[i + 2] * h[i + 2] + h[i + 3] * h[i + 3]); }
;             s = wave_sum(s);
.LBB0_1421:
	s_waitcnt vmcnt(6)
.Ln2_enter:
	v_mov_b64_e32 v[46:47], v[64:65]
	v_mov_b64_e32 v[48:49], v[66:67]
	v_mov_b64_e32 v[50:51], v[68:69]
	v_mov_b64_e32 v[52:53], v[70:71]
	v_mov_b64_e32 v[54:55], v[72:73]
	v_mov_b64_e32 v[56:57], v[74:75]
	v_mov_b64_e32 v[26:27], v[76:77]
	v_mov_b64_e32 v[28:29], v[78:79]
	v_mov_b64_e32 v[34:35], v[80:81]
	v_mov_b64_e32 v[36:37], v[82:83]
	v_mov_b64_e32 v[30:31], v[84:85]
	v_mov_b64_e32 v[32:33], v[86:87]
	v_mov_b64_e32 v[14:15], v[88:89]
	v_mov_b64_e32 v[16:17], v[90:91]
	v_mov_b64_e32 v[22:23], v[92:93]
	v_mov_b64_e32 v[24:25], v[94:95]
	v_mov_b64_e32 v[18:19], v[98:99]
	v_mov_b64_e32 v[20:21], v[100:101]
	v_mov_b64_e32 v[2:3], v[102:103]
	v_mov_b64_e32 v[4:5], v[104:105]
	v_mov_b64_e32 v[6:7], v[106:107]
	v_mov_b64_e32 v[8:9], v[108:109]
	v_mov_b64_e32 v[10:11], v[110:111]
	v_mov_b64_e32 v[12:13], v[112:113]
	v_lshl_add_u64 v[42:43], s[74:75], 0, v[40:41]
	v_add_co_u32_e32 v44, vcc, 0xee00000, v42
	s_nop 1
	v_addc_co_u32_e32 v45, vcc, 0, v43, vcc
	v_readlane_b32 s3, v254, 47
	s_nop 0
	s_add_i32 s3, s2, s3
	s_cmp_lt_i32 s3, 0x8000
	s_cbranch_scc0 .Ln2_nopf
	v_readlane_b32 s6, v254, 49
	v_readlane_b32 s7, v254, 50
	s_nop 1
	v_lshl_add_u64 v[114:115], v[40:41], 0, s[6:7]
	v_readlane_b32 s6, v254, 41
	v_readlane_b32 s7, v254, 42
	s_nop 1
	v_lshl_add_u64 v[118:119], v[38:39], 0, s[6:7]
	v_lshl_add_u64 v[116:117], s[74:75], 0, v[114:115]
	v_add_co_u32_e32 v116, vcc, 0xee00000, v116
	s_nop 1
	v_addc_co_u32_e32 v117, vcc, 0, v117, vcc
	v_lshl_add_u64 v[122:123], s[74:75], 0, v[118:119]
	v_add_co_u32_e32 v124, vcc, 0x15200000, v122
	s_nop 1
	v_addc_co_u32_e32 v125, vcc, 0, v123, vcc
	s_mov_b32 s3, 0x15201000
	v_add_co_u32_e32 v126, vcc, s3, v122
	s_nop 1
	v_addc_co_u32_e32 v127, vcc, 0, v123, vcc
	global_load_dwordx4 v[64:67], v[116:117], off
	global_load_dwordx4 v[68:71], v[124:125], off
	global_load_dwordx4 v[72:75], v[124:125], off offset:2048
	global_load_dwordx4 v[76:79], v[116:117], off offset:1024
	global_load_dwordx4 v[80:83], v[124:125], off offset:1024
	global_load_dwordx4 v[84:87], v[124:125], off offset:3072
	global_load_dwordx4 v[88:91], v[116:117], off offset:2048
	global_load_dwordx4 v[92:95], v[126:127], off
	global_load_dwordx4 v[98:101], v[126:127], off offset:2048
	global_load_dwordx4 v[102:105], v[116:117], off offset:3072
	global_load_dwordx4 v[106:109], v[126:127], off offset:1024
	global_load_dwordx4 v[110:113], v[126:127], off offset:3072
.Ln2_nopf:
	v_lshlrev_b32_e32 v58, 16, v46
	v_lshlrev_b32_e32 v60, 16, v50
	v_and_b32_e32 v61, 0xffff0000, v50
	v_lshlrev_b32_e32 v62, 16, v54
	v_and_b32_e32 v63, 0xffff0000, v54
	v_and_b32_e32 v59, 0xffff0000, v46
	v_pk_add_f32 v[60:61], v[60:61], v[62:63]
	v_lshlrev_b32_e32 v50, 16, v51
	v_and_b32_e32 v51, 0xffff0000, v51
	v_lshlrev_b32_e32 v54, 16, v55
	v_and_b32_e32 v55, 0xffff0000, v55
	v_pk_add_f32 v[58:59], v[60:61], v[58:59]
	v_lshlrev_b32_e32 v46, 16, v47
	v_and_b32_e32 v47, 0xffff0000, v47
	v_pk_add_f32 v[50:51], v[50:51], v[54:55]
	v_lshlrev_b32_e32 v54, 16, v52
	v_and_b32_e32 v55, 0xffff0000, v52
	v_lshlrev_b32_e32 v60, 16, v56
	v_and_b32_e32 v61, 0xffff0000, v56
	v_pk_add_f32 v[50:51], v[50:51], v[46:47]
	v_lshlrev_b32_e32 v46, 16, v48
	v_and_b32_e32 v47, 0xffff0000, v48
	v_pk_add_f32 v[54:55], v[54:55], v[60:61]
	v_lshlrev_b32_e32 v48, 16, v53
	v_pk_add_f32 v[54:55], v[54:55], v[46:47]
	v_lshlrev_b32_e32 v46, 16, v49
	v_and_b32_e32 v47, 0xffff0000, v49
	v_and_b32_e32 v49, 0xffff0000, v53
	v_lshlrev_b32_e32 v52, 16, v57
	v_and_b32_e32 v53, 0xffff0000, v57
	v_pk_add_f32 v[48:49], v[48:49], v[52:53]
	s_nop 0
	v_pk_add_f32 v[52:53], v[48:49], v[46:47]
	v_cvt_pk_bf16_f32 v46, v58, v59
	v_cvt_pk_bf16_f32 v47, v50, v51
	v_cvt_pk_bf16_f32 v48, v54, v55
	v_cvt_pk_bf16_f32 v49, v52, v53
	global_store_dwordx4 v[44:45], v[46:49], off
	v_lshlrev_b32_e32 v0, 16, v46
	v_lshlrev_b32_e32 v50, 16, v47
	v_and_b32_e32 v46, 0xffff0000, v46
	v_and_b32_e32 v47, 0xffff0000, v47
	v_mul_f32_e32 v46, v46, v46
	v_fmac_f32_e32 v46, v0, v0
	v_mul_f32_e32 v0, v47, v47
	v_lshlrev_b32_e32 v51, 16, v48
	v_and_b32_e32 v48, 0xffff0000, v48
	v_lshlrev_b32_e32 v52, 16, v49
	v_and_b32_e32 v49, 0xffff0000, v49
	v_fmac_f32_e32 v0, v50, v50
	v_add_f32_e32 v0, v46, v0
	v_mul_f32_e32 v46, v48, v48
	v_mul_f32_e32 v47, v49, v49
	v_fmac_f32_e32 v46, v51, v51
	v_fmac_f32_e32 v47, v52, v52
	v_add_f32_e32 v46, v46, v47
	v_lshlrev_b32_e32 v48, 16, v34
	v_and_b32_e32 v49, 0xffff0000, v34
	v_lshlrev_b32_e32 v50, 16, v30
	v_and_b32_e32 v51, 0xffff0000, v30
	v_add_f32_e32 v0, v0, v46
	v_lshlrev_b32_e32 v46, 16, v26
	v_and_b32_e32 v47, 0xffff0000, v26
	v_pk_add_f32 v[48:49], v[48:49], v[50:51]
	v_lshlrev_b32_e32 v34, 16, v35
	v_and_b32_e32 v35, 0xffff0000, v35
	v_lshlrev_b32_e32 v30, 16, v31
	v_and_b32_e32 v31, 0xffff0000, v31
	v_pk_add_f32 v[46:47], v[48:49], v[46:47]
	v_lshlrev_b32_e32 v26, 16, v27
	v_and_b32_e32 v27, 0xffff0000, v27
	v_pk_add_f32 v[30:31], v[34:35], v[30:31]
	v_lshlrev_b32_e32 v34, 16, v36
	v_and_b32_e32 v35, 0xffff0000, v36
	v_lshlrev_b32_e32 v48, 16, v32
	v_and_b32_e32 v49, 0xffff0000, v32
	v_pk_add_f32 v[30:31], v[30:31], v[26:27]
	v_lshlrev_b32_e32 v26, 16, v28
	v_and_b32_e32 v27, 0xffff0000, v28
	v_pk_add_f32 v[34:35], v[34:35], v[48:49]
	v_lshlrev_b32_e32 v28, 16, v37
	v_pk_add_f32 v[34:35], v[34:35], v[26:27]
	v_lshlrev_b32_e32 v26, 16, v29
	v_and_b32_e32 v27, 0xffff0000, v29
	v_and_b32_e32 v29, 0xffff0000, v37
	v_lshlrev_b32_e32 v32, 16, v33
	v_and_b32_e32 v33, 0xffff0000, v33
	v_pk_add_f32 v[28:29], v[28:29], v[32:33]
	s_nop 0
	v_pk_add_f32 v[32:33], v[28:29], v[26:27]
	v_cvt_pk_bf16_f32 v26, v46, v47
	v_cvt_pk_bf16_f32 v27, v30, v31
	v_cvt_pk_bf16_f32 v28, v34, v35
	v_cvt_pk_bf16_f32 v29, v32, v33
	global_store_dwordx4 v[44:45], v[26:29], off offset:1024
	v_lshlrev_b32_e32 v30, 16, v26
	v_lshlrev_b32_e32 v31, 16, v27
	v_and_b32_e32 v26, 0xffff0000, v26
	v_and_b32_e32 v27, 0xffff0000, v27
	v_mul_f32_e32 v26, v26, v26
	v_mul_f32_e32 v27, v27, v27
	v_fmac_f32_e32 v26, v30, v30
	v_fmac_f32_e32 v27, v31, v31
	v_lshlrev_b32_e32 v32, 16, v28
	v_and_b32_e32 v28, 0xffff0000, v28
	v_lshlrev_b32_e32 v33, 16, v29
	v_and_b32_e32 v29, 0xffff0000, v29
	v_add_f32_e32 v26, v26, v27
	v_add_f32_e32 v0, v0, v26
	v_mul_f32_e32 v26, v28, v28
	v_mul_f32_e32 v27, v29, v29
	v_fmac_f32_e32 v26, v32, v32
	v_fmac_f32_e32 v27, v33, v33
	v_add_f32_e32 v26, v26, v27
	v_add_f32_e32 v0, v26, v0
	s_nop 1
	v_add_f32_dpp v0, v0, v0 quad_perm:[1,0,3,2] row_mask:0xf bank_mask:0xf bound_ctrl:1
	s_nop 1
	v_add_f32_dpp v0, v0, v0 quad_perm:[2,3,0,1] row_mask:0xf bank_mask:0xf bound_ctrl:1
	s_nop 1
	v_add_f32_dpp v0, v0, v0 row_half_mirror row_mask:0xf bank_mask:0xf bound_ctrl:1
	s_nop 1
	v_add_f32_dpp v0, v0, v0 row_mirror row_mask:0xf bank_mask:0xf bound_ctrl:1
	s_nop 0
	v_readlane_b32 s12, v0, 0
	v_readlane_b32 s3, v0, 16
	v_readlane_b32 s13, v0, 32
	v_readlane_b32 s6, v0, 48
	s_and_saveexec_b64 s[16:17], s[10:11]
	s_cbranch_execz .LBB0_1423
; __device__ __forceinline__ void phase_norm2(Frame& F, int l, float ysc) {
;     ...
;             s = wave_sum(s);
;             if (F.lane == 0) RS[row0 + q] = 1.0f / sqrtf(s * (1.f / DM) + EPS); }
	v_mov_b32_e32 v26, s3
	v_mov_b32_e32 v27, s6
	v_pk_add_f32 v[26:27], s[12:13], v[26:27]
	s_mov_b32 s3, 0xf800000
	v_add_f32_e32 v0, v26, v27
	v_fmamk_f32 v0, v0, 0x3a800000, v236
	v_mul_f32_e32 v26, 0x4f800000, v0
	v_cmp_gt_f32_e32 vcc, s3, v0
	s_add_u32 s3, s74, s14
	s_nop 0
	v_cndmask_b32_e32 v0, v0, v26, vcc
	v_sqrt_f32_e32 v26, v0
	s_nop 0
	v_add_u32_e32 v27, -1, v26
	v_fma_f32 v28, -v27, v26, v0
	v_cmp_ge_f32_e64 s[12:13], 0, v28
	v_add_u32_e32 v28, 1, v26
	s_nop 0
	v_cndmask_b32_e64 v27, v26, v27, s[12:13]
	v_fma_f32 v26, -v28, v26, v0
	v_cmp_lt_f32_e64 s[12:13], 0, v26
	s_nop 1
	v_cndmask_b32_e64 v26, v27, v28, s[12:13]
	v_mul_f32_e32 v27, 0x37800000, v26
	v_cndmask_b32_e32 v26, v26, v27, vcc
	v_cmp_class_f32_e32 vcc, v0, v251
	s_nop 1
	v_cndmask_b32_e32 v0, v26, v0, vcc
	v_div_scale_f32 v26, s[6:7], v0, v0, 1.0
	v_rcp_f32_e32 v27, v26
	s_addc_u32 s6, s75, s15
	v_fma_f32 v28, -v26, v27, 1.0
	v_fmac_f32_e32 v27, v28, v27
	v_div_scale_f32 v28, vcc, 1.0, v0, 1.0
	v_mul_f32_e32 v29, v28, v27
	v_fma_f32 v30, -v26, v29, v28
	v_fmac_f32_e32 v29, v30, v27
	v_fma_f32 v26, -v26, v29, v28
	v_div_fmas_f32 v26, v26, v27, v29
	v_div_fixup_f32 v0, v26, v0, 1.0
	v_mov_b32_e32 v26, s3
	v_add_co_u32_e32 v26, vcc, 0x500000, v26
	v_mov_b32_e32 v27, s6
	s_nop 0
	v_addc_co_u32_e32 v27, vcc, 0, v27, vcc
	global_store_dword v[26:27], v0, off
; __device__ __forceinline__ unsigned pk2(float lo, float hi) { f32x2_cv_ v = {lo, hi}; return __builtin_bit_cast(unsigned, __builtin_convertvector(v, bf16x2_cv_)); }
; __device__ __forceinline__ void phase_norm2(Frame& F, int l, float ysc) {
;     ...
;         for (int q = 0; q < 2; ++q) { float s = 0.f; u32x4* xr = (u32x4*)(HB + (size_t)(row0 + q) * DM) + F.lane;
; #pragma unroll
;             for (int j = 0; j < 2; ++j) { float h[8], a[8], b[8]; unpack8(hw[q][j], h); unpack8(ya[q][j], a); unpack8(yb[q][j], b);
; #pragma unroll
;                 for (int i = 0; i < 8; ++i) h[i] += ysc * (a[i] + b[i]);
;                 const u32x4 o = (u32x4){pk2(h[0], h[1]), pk2(h[2], h[3]), pk2(h[4], h[5]), pk2(h[6], h[7])}; xr[64 * j] = o;
;                 unpack8(o, h);
; #pragma unroll
;                 for (int i = 0; i < 8; i += 4) s += (h[i] * h[i] + h[i + 1] * h[i + 1]) + (h[i + 2] * h[i + 2] + h[i + 3] * h[i + 3]); }
;             s = wave_sum(s);
;             if (F.lane == 0) RS[row0 + q] = 1.0f / sqrtf(s * (1.f / DM) + EPS); }
.LBB0_1423:
	s_or_b64 exec, exec, s[16:17]
	v_lshlrev_b32_e32 v32, 16, v22
	v_and_b32_e32 v33, 0xffff0000, v22
	v_lshlrev_b32_e32 v34, 16, v18
	v_and_b32_e32 v35, 0xffff0000, v18
	v_lshlrev_b32_e32 v30, 16, v14
	v_and_b32_e32 v31, 0xffff0000, v14
	v_pk_add_f32 v[32:33], v[32:33], v[34:35]
	v_lshlrev_b32_e32 v22, 16, v23
	v_and_b32_e32 v23, 0xffff0000, v23
	v_lshlrev_b32_e32 v18, 16, v19
	v_and_b32_e32 v19, 0xffff0000, v19
	v_pk_add_f32 v[30:31], v[32:33], v[30:31]
	v_lshlrev_b32_e32 v14, 16, v15
	v_and_b32_e32 v15, 0xffff0000, v15
	v_pk_add_f32 v[18:19], v[22:23], v[18:19]
	v_lshlrev_b32_e32 v22, 16, v24
	v_and_b32_e32 v23, 0xffff0000, v24
	v_lshlrev_b32_e32 v32, 16, v20
	v_and_b32_e32 v33, 0xffff0000, v20
	v_pk_add_f32 v[18:19], v[18:19], v[14:15]
	v_lshlrev_b32_e32 v14, 16, v16
	v_and_b32_e32 v15, 0xffff0000, v16
	v_pk_add_f32 v[22:23], v[22:23], v[32:33]
	v_lshlrev_b32_e32 v16, 16, v25
	v_pk_add_f32 v[22:23], v[22:23], v[14:15]
	v_lshlrev_b32_e32 v14, 16, v17
	v_and_b32_e32 v15, 0xffff0000, v17
	v_and_b32_e32 v17, 0xffff0000, v25
	v_lshlrev_b32_e32 v20, 16, v21
	v_and_b32_e32 v21, 0xffff0000, v21
	v_pk_add_f32 v[16:17], v[16:17], v[20:21]
	s_mov_b64 s[6:7], 0xee00800
	v_pk_add_f32 v[20:21], v[16:17], v[14:15]
	v_lshl_add_u64 v[26:27], v[42:43], 0, s[6:7]
	v_cvt_pk_bf16_f32 v14, v30, v31
	v_cvt_pk_bf16_f32 v15, v18, v19
	v_cvt_pk_bf16_f32 v16, v22, v23
	v_cvt_pk_bf16_f32 v17, v20, v21
	global_store_dwordx4 v[26:27], v[14:17], off
	v_lshlrev_b32_e32 v0, 16, v14
	v_lshlrev_b32_e32 v18, 16, v15
	v_and_b32_e32 v14, 0xffff0000, v14
	v_and_b32_e32 v15, 0xffff0000, v15
	v_mul_f32_e32 v14, v14, v14
	v_fmac_f32_e32 v14, v0, v0
	v_mul_f32_e32 v0, v15, v15
	v_lshlrev_b32_e32 v19, 16, v16
	v_and_b32_e32 v16, 0xffff0000, v16
	v_lshlrev_b32_e32 v20, 16, v17
	v_and_b32_e32 v17, 0xffff0000, v17
	v_fmac_f32_e32 v0, v18, v18
	v_add_f32_e32 v0, v14, v0
	v_mul_f32_e32 v14, v16, v16
	v_mul_f32_e32 v15, v17, v17
	v_fmac_f32_e32 v14, v19, v19
	v_fmac_f32_e32 v15, v20, v20
	v_add_f32_e32 v14, v14, v15
	v_lshlrev_b32_e32 v16, 16, v6
	v_and_b32_e32 v17, 0xffff0000, v6
	v_lshlrev_b32_e32 v18, 16, v10
	v_and_b32_e32 v19, 0xffff0000, v10
	v_add_f32_e32 v0, v0, v14
	v_lshlrev_b32_e32 v14, 16, v2
	v_and_b32_e32 v15, 0xffff0000, v2
	v_pk_add_f32 v[16:17], v[16:17], v[18:19]
	v_lshlrev_b32_e32 v6, 16, v7
	v_and_b32_e32 v7, 0xffff0000, v7
	v_lshlrev_b32_e32 v10, 16, v11
	v_and_b32_e32 v11, 0xffff0000, v11
	v_pk_add_f32 v[14:15], v[16:17], v[14:15]
	v_lshlrev_b32_e32 v2, 16, v3
	v_and_b32_e32 v3, 0xffff0000, v3
	v_pk_add_f32 v[6:7], v[6:7], v[10:11]
	v_lshlrev_b32_e32 v10, 16, v8
	v_and_b32_e32 v11, 0xffff0000, v8
	v_lshlrev_b32_e32 v16, 16, v12
	v_and_b32_e32 v17, 0xffff0000, v12
	v_pk_add_f32 v[6:7], v[6:7], v[2:3]
	v_lshlrev_b32_e32 v2, 16, v4
	v_and_b32_e32 v3, 0xffff0000, v4
	v_pk_add_f32 v[10:11], v[10:11], v[16:17]
	v_lshlrev_b32_e32 v4, 16, v9
	v_pk_add_f32 v[10:11], v[10:11], v[2:3]
	v_lshlrev_b32_e32 v2, 16, v5
	v_and_b32_e32 v3, 0xffff0000, v5
	v_and_b32_e32 v5, 0xffff0000, v9
	v_lshlrev_b32_e32 v8, 16, v13
	v_and_b32_e32 v9, 0xffff0000, v13
	v_pk_add_f32 v[4:5], v[4:5], v[8:9]
	s_mov_b64 s[6:7], 0xee00c00
	v_pk_add_f32 v[8:9], v[4:5], v[2:3]
	v_lshl_add_u64 v[28:29], v[42:43], 0, s[6:7]
	v_cvt_pk_bf16_f32 v2, v14, v15
	v_cvt_pk_bf16_f32 v3, v6, v7
	v_cvt_pk_bf16_f32 v4, v10, v11
	v_cvt_pk_bf16_f32 v5, v8, v9
	global_store_dwordx4 v[28:29], v[2:5], off
	v_lshlrev_b32_e32 v6, 16, v2
	v_lshlrev_b32_e32 v7, 16, v3
	v_and_b32_e32 v2, 0xffff0000, v2
	v_and_b32_e32 v3, 0xffff0000, v3
	v_mul_f32_e32 v2, v2, v2
	v_mul_f32_e32 v3, v3, v3
	v_fmac_f32_e32 v2, v6, v6
	v_fmac_f32_e32 v3, v7, v7
	v_lshlrev_b32_e32 v8, 16, v4
	v_and_b32_e32 v4, 0xffff0000, v4
	v_lshlrev_b32_e32 v9, 16, v5
	v_and_b32_e32 v5, 0xffff0000, v5
	v_add_f32_e32 v2, v2, v3
	v_add_f32_e32 v0, v0, v2
	v_mul_f32_e32 v2, v4, v4
	v_mul_f32_e32 v3, v5, v5
	v_fmac_f32_e32 v2, v8, v8
	v_fmac_f32_e32 v3, v9, v9
	v_add_f32_e32 v2, v2, v3
	v_add_f32_e32 v0, v2, v0
	s_nop 1
	v_add_f32_dpp v0, v0, v0 quad_perm:[1,0,3,2] row_mask:0xf bank_mask:0xf bound_ctrl:1
	s_nop 1
	v_add_f32_dpp v0, v0, v0 quad_perm:[2,3,0,1] row_mask:0xf bank_mask:0xf bound_ctrl:1
	s_nop 1
	v_add_f32_dpp v0, v0, v0 row_half_mirror row_mask:0xf bank_mask:0xf bound_ctrl:1
	s_nop 1
	v_add_f32_dpp v0, v0, v0 row_mirror row_mask:0xf bank_mask:0xf bound_ctrl:1
	s_nop 0
	v_readlane_b32 s12, v0, 0
	v_readlane_b32 s3, v0, 16
	v_readlane_b32 s13, v0, 32
	v_readlane_b32 s6, v0, 48
	s_and_saveexec_b64 s[16:17], s[10:11]
	s_cbranch_execz .LBB0_1420
	v_mov_b32_e32 v2, s3
	v_mov_b32_e32 v3, s6
	v_pk_add_f32 v[2:3], s[12:13], v[2:3]
	s_mov_b32 s3, 0xf800000
	v_add_f32_e32 v0, v2, v3
	v_fmamk_f32 v0, v0, 0x3a800000, v236
	v_mul_f32_e32 v2, 0x4f800000, v0
	v_cmp_gt_f32_e32 vcc, s3, v0
	s_add_u32 s3, s74, s14
	s_nop 0
	v_cndmask_b32_e32 v0, v0, v2, vcc
	v_sqrt_f32_e32 v2, v0
	s_nop 0
	v_add_u32_e32 v3, -1, v2
	v_fma_f32 v4, -v3, v2, v0
	v_cmp_ge_f32_e64 s[12:13], 0, v4
	v_add_u32_e32 v4, 1, v2
	s_nop 0
	v_cndmask_b32_e64 v3, v2, v3, s[12:13]
	v_fma_f32 v2, -v4, v2, v0
	v_cmp_lt_f32_e64 s[12:13], 0, v2
	s_nop 1
	v_cndmask_b32_e64 v2, v3, v4, s[12:13]
	v_mul_f32_e32 v3, 0x37800000, v2
	v_cndmask_b32_e32 v2, v2, v3, vcc
	v_cmp_class_f32_e32 vcc, v0, v251
	s_nop 1
	v_cndmask_b32_e32 v0, v2, v0, vcc
	v_div_scale_f32 v2, s[6:7], v0, v0, 1.0
	v_rcp_f32_e32 v3, v2
	s_addc_u32 s6, s75, s15
	v_fma_f32 v4, -v2, v3, 1.0
	v_fmac_f32_e32 v3, v4, v3
	v_div_scale_f32 v4, vcc, 1.0, v0, 1.0
	v_mul_f32_e32 v5, v4, v3
	v_fma_f32 v6, -v2, v5, v4
	v_fmac_f32_e32 v5, v6, v3
	v_fma_f32 v2, -v2, v5, v4
	v_div_fmas_f32 v2, v2, v3, v5
	v_div_fixup_f32 v0, v2, v0, 1.0
	v_mov_b32_e32 v2, s3
	v_add_co_u32_e32 v2, vcc, 0x500000, v2
	v_mov_b32_e32 v3, s6
	s_nop 0
	v_addc_co_u32_e32 v3, vcc, 0, v3, vcc
	global_store_dword v[2:3], v0, off offset:4
	s_branch .LBB0_1420
